# k_gcn: rowptr load issued ahead of weight-fragment loads (shorter start-up dependency chain)
# speedup vs baseline: 1.0168x; 1.0006x over previous
_Z5k_gcnILi128ELb1ELi16EEvPKDv8_DF16_PKiS4_PKfS2_S6_PDF16_S6_S6_S2_S6_S2_S6_S6_S6_PfS4_:
	s_load_dwordx4 s[20:23], s[0:1], 0x8
	s_load_dwordx2 s[4:5], s[0:1], 0x20
	v_readfirstlane_b32 s30, v0
	v_and_b32_e32 v1, 63, v0
	s_lshr_b32 s28, s30, 6
	v_lshl_or_b32 v2, s28, 9, v1
	v_mov_b32_e32 v3, 0
	v_bfe_u32 v83, v0, 4, 2
	s_waitcnt lgkmcnt(0)
	v_lshl_add_u64 v[14:15], v[2:3], 4, s[4:5]
	v_ashrrev_i32_e32 v3, 31, v2
	s_lshl_b32 s29, s2, 4
	s_lshl_b32 s6, s28, 2
	v_or_b32_e32 v38, s29, v83
	v_add_lshl_u32 v38, v38, s6, 2
	global_load_dwordx2 v[50:51], v38, s[20:21]
	v_lshl_add_u64 v[16:17], v[2:3], 4, s[4:5]
	global_load_dwordx4 v[26:29], v[14:15], off
	global_load_dwordx4 v[10:13], v[16:17], off offset:1024
	global_load_dwordx4 v[6:9], v[16:17], off offset:2048
	global_load_dwordx4 v[2:5], v[16:17], off offset:3072
	v_or_b32_e32 v14, s29, v83
	s_lshl_b32 s6, s28, 2
	v_add_u32_e32 v14, s6, v14
	s_movk_i32 s3, 0x1000
	v_ashrrev_i32_e32 v15, 31, v14
	v_add_co_u32_e32 v34, vcc, s3, v16
	v_lshl_add_u64 v[36:37], v[14:15], 2, s[20:21]
	s_nop 0
	v_addc_co_u32_e32 v35, vcc, 0, v17, vcc
	global_load_dwordx4 v[30:33], v[34:35], off
	global_load_dwordx4 v[22:25], v[34:35], off offset:1024
	global_load_dwordx4 v[18:21], v[34:35], off offset:2048
	global_load_dwordx4 v[14:17], v[34:35], off offset:3072
	s_waitcnt vmcnt(8)
	v_sub_u32_e32 v53, v51, v50
	v_lshlrev_b32_e32 v34, 2, v50
	global_load_dword v36, v34, s[22:23]
	global_load_dword v38, v34, s[22:23] offset:4
	global_load_dword v42, v34, s[22:23] offset:8
	global_load_dword v46, v34, s[22:23] offset:12
	s_load_dwordx2 s[24:25], s[0:1], 0x0
	s_load_dwordx2 s[2:3], s[0:1], 0x18
	v_and_b32_e32 v82, 15, v0
	v_or_b32_e32 v51, s6, v83
	v_add_u32_e32 v34, s29, v51
	v_lshlrev_b32_e32 v54, 4, v82
	s_mov_b32 s27, 0x20000
	s_mov_b32 s26, 0x4e2100
	s_waitcnt lgkmcnt(0)
	s_and_b32 s25, s25, 0xffff
	v_lshl_or_b32 v35, v34, 8, v54
	buffer_load_dwordx4 v[64:67], v35, s[24:27], 0 offen
	v_ashrrev_i32_e32 v35, 31, v34
	v_lshl_add_u64 v[34:35], v[34:35], 2, s[2:3]
	global_load_dword v52, v[34:35], off
	v_mbcnt_lo_u32_b32 v34, -1, 0
	v_mbcnt_hi_u32_b32 v34, -1, v34
	v_and_b32_e32 v37, 64, v34
	v_xor_b32_e32 v35, 32, v34
	v_add_u32_e32 v37, 64, v37
	v_cmp_lt_i32_e32 vcc, v35, v37
	v_xor_b32_e32 v39, 16, v34
	s_load_dwordx2 s[2:3], s[0:1], 0x78
	s_load_dwordx8 s[4:11], s[0:1], 0x58
	s_load_dwordx8 s[12:19], s[0:1], 0x38
	v_cndmask_b32_e32 v35, v34, v35, vcc
	v_lshlrev_b32_e32 v84, 2, v35
	ds_bpermute_b32 v35, v84, v53
	v_cmp_lt_i32_e32 vcc, v39, v37
	s_mov_b32 s33, 4
	s_waitcnt vmcnt(1)
	v_mov_b32_e32 v70, 0x4e20
	v_cmp_lt_i32_e64 s[34:35], 0, v53
	v_cmp_lt_i32_e64 s[36:37], 1, v53
	v_cmp_lt_i32_e64 s[38:39], 2, v53
	v_cmp_lt_i32_e64 s[40:41], 3, v53
	v_cndmask_b32_e64 v36, v70, v36, s[34:35]
	v_cndmask_b32_e64 v38, v70, v38, s[36:37]
	v_cndmask_b32_e64 v42, v70, v42, s[38:39]
	v_cndmask_b32_e64 v46, v70, v46, s[40:41]
	v_cvt_f32_f16_e32 v62, v64
	v_cndmask_b32_e32 v34, v34, v39, vcc
	v_lshlrev_b32_e32 v85, 2, v34
	s_waitcnt lgkmcnt(0)
	v_max_i32_e32 v34, v53, v35
	ds_bpermute_b32 v35, v85, v34
	v_cvt_f32_f16_sdwa v63, v64 dst_sel:DWORD dst_unused:UNUSED_PAD src0_sel:WORD_1
	v_cvt_f32_f16_e32 v60, v65
	v_cvt_f32_f16_sdwa v61, v65 dst_sel:DWORD dst_unused:UNUSED_PAD src0_sel:WORD_1
	v_cvt_f32_f16_e32 v58, v66
	v_cvt_f32_f16_sdwa v59, v66 dst_sel:DWORD dst_unused:UNUSED_PAD src0_sel:WORD_1
	v_cvt_f32_f16_e32 v56, v67
	v_cvt_f32_f16_sdwa v57, v67 dst_sel:DWORD dst_unused:UNUSED_PAD src0_sel:WORD_1
	s_waitcnt lgkmcnt(0)
	v_max_i32_e32 v34, v34, v35
	s_nop 0
	v_readfirstlane_b32 s31, v34
	s_cmp_lt_i32 s31, 1
	s_cbranch_scc1 .LBB2_19
